# stacked + expert GEMM1 epilogue: fp8 output scale (x4) folded exactly into the (u+1) step as one packed fma, 32 fewer packed multiplies per unit
# baseline (speedup 1.0000x reference)
.LBB0_1485:
	s_lshl_b32 s1, s30, 7
	s_ashr_i32 s0, s30, 4
	s_and_b32 s1, s1, 0x780
	v_or_b32_e32 v170, s1, v184
	v_lshl_add_u32 v20, s28, 8, v182
	s_mov_b32 s98, 0x3a800000
	s_mov_b32 s99, 0x3fd9db23
	s_mov_b32 s100, 0xbfb8aa3b
	s_mov_b32 s101, 4.0
	v_ashrrev_i32_e32 v21, 31, v20
	v_mov_b32_e32 v12, v170
	v_mov_b32_e32 v13, 0
	v_mov_b32_e32 v15, 0
	v_mov_b32_e32 v16, 1.0
	v_mov_b32_e32 v17, 1.0
	v_mov_b32_e32 v10, 4.0
	v_mov_b32_e32 v11, 4.0
	v_lshlrev_b64 v[18:19], 11, v[20:21]
	v_lshl_add_u64 v[18:19], s[14:15], 0, v[18:19]
	v_lshl_add_u64 v[18:19], v[18:19], 0, v[12:13]
	v_pk_fma_f32 v[158:159], v[158:159], s[98:99], v[224:225] op_sel_hi:[1,0,1]
	v_pk_fma_f32 v[160:161], v[160:161], s[98:99], v[226:227] op_sel_hi:[1,0,1]
	v_pk_fma_f32 v[154:155], v[154:155], s[98:99], v[228:229] op_sel_hi:[1,0,1]
	v_pk_fma_f32 v[156:157], v[156:157], s[98:99], v[230:231] op_sel_hi:[1,0,1]
	v_pk_fma_f32 v[150:151], v[150:151], s[98:99], v[232:233] op_sel_hi:[1,0,1]
	v_pk_fma_f32 v[152:153], v[152:153], s[98:99], v[234:235] op_sel_hi:[1,0,1]
	v_pk_fma_f32 v[146:147], v[146:147], s[98:99], v[236:237] op_sel_hi:[1,0,1]
	v_pk_fma_f32 v[148:149], v[148:149], s[98:99], v[238:239] op_sel_hi:[1,0,1]
	v_min_f32_e32 v158, 0x40e00000, v158
	v_min_f32_e32 v159, 0x40e00000, v159
	v_min_f32_e32 v160, 0x40e00000, v160
	v_min_f32_e32 v161, 0x40e00000, v161
	v_min_f32_e32 v154, 0x40e00000, v154
	v_min_f32_e32 v155, 0x40e00000, v155
	v_min_f32_e32 v156, 0x40e00000, v156
	v_min_f32_e32 v157, 0x40e00000, v157
	v_med3_f32 v150, v150, s59, v189
	v_med3_f32 v151, v151, s59, v189
	v_med3_f32 v152, v152, s59, v189
	v_med3_f32 v153, v153, s59, v189
	v_med3_f32 v146, v146, s59, v189
	v_med3_f32 v147, v147, s59, v189
	v_med3_f32 v148, v148, s59, v189
	v_med3_f32 v149, v149, s59, v189
	v_pk_mul_f32 v[2:3], v[158:159], s[98:99] op_sel:[0,1]
	v_pk_mul_f32 v[4:5], v[160:161], s[98:99] op_sel:[0,1]
	v_pk_mul_f32 v[6:7], v[154:155], s[98:99] op_sel:[0,1]
	v_pk_mul_f32 v[8:9], v[156:157], s[98:99] op_sel:[0,1]
	v_pk_mul_f32 v[2:3], v[2:3], s[100:101] op_sel_hi:[1,0]
	v_pk_mul_f32 v[4:5], v[4:5], s[100:101] op_sel_hi:[1,0]
	v_pk_mul_f32 v[6:7], v[6:7], s[100:101] op_sel_hi:[1,0]
	v_pk_mul_f32 v[8:9], v[8:9], s[100:101] op_sel_hi:[1,0]
	v_exp_f32_e32 v2, v2
	v_exp_f32_e32 v3, v3
	v_exp_f32_e32 v4, v4
	v_exp_f32_e32 v5, v5
	v_exp_f32_e32 v6, v6
	v_exp_f32_e32 v7, v7
	v_exp_f32_e32 v8, v8
	v_exp_f32_e32 v9, v9
	v_pk_fma_f32 v[150:151], v[150:151], s[100:101], v[10:11] op_sel:[0,1,0]
	v_pk_fma_f32 v[152:153], v[152:153], s[100:101], v[10:11] op_sel:[0,1,0]
	v_pk_fma_f32 v[146:147], v[146:147], s[100:101], v[10:11] op_sel:[0,1,0]
	v_pk_fma_f32 v[148:149], v[148:149], s[100:101], v[10:11] op_sel:[0,1,0]
	v_pk_add_f32 v[2:3], v[2:3], v[16:17]
	v_pk_add_f32 v[4:5], v[4:5], v[16:17]
	v_pk_add_f32 v[6:7], v[6:7], v[16:17]
	v_pk_add_f32 v[8:9], v[8:9], v[16:17]
	v_pk_mul_f32 v[158:159], v[158:159], v[150:151]
	v_pk_mul_f32 v[160:161], v[160:161], v[152:153]
	v_pk_mul_f32 v[154:155], v[154:155], v[146:147]
	v_pk_mul_f32 v[156:157], v[156:157], v[148:149]
	v_rcp_f32_e32 v2, v2
	v_rcp_f32_e32 v3, v3
	v_rcp_f32_e32 v4, v4
	v_rcp_f32_e32 v5, v5
	v_rcp_f32_e32 v6, v6
	v_rcp_f32_e32 v7, v7
	v_rcp_f32_e32 v8, v8
	v_rcp_f32_e32 v9, v9
	s_nop 1
	v_pk_mul_f32 v[158:159], v[158:159], v[2:3]
	v_pk_mul_f32 v[160:161], v[160:161], v[4:5]
	v_pk_mul_f32 v[154:155], v[154:155], v[6:7]
	v_pk_mul_f32 v[156:157], v[156:157], v[8:9]
	v_cvt_pk_fp8_f32 v22, v158, v159
	v_cvt_pk_fp8_f32 v23, v154, v155
	v_cvt_pk_fp8_f32 v22, v160, v161 op_sel:[0,0,1]
	v_cvt_pk_fp8_f32 v23, v156, v157 op_sel:[0,0,1]
	global_store_dwordx2 v[18:19], v[22:23], off
	v_pk_fma_f32 v[142:143], v[142:143], s[98:99], v[224:225] op_sel_hi:[1,0,1]
	v_pk_fma_f32 v[144:145], v[144:145], s[98:99], v[226:227] op_sel_hi:[1,0,1]
	v_pk_fma_f32 v[138:139], v[138:139], s[98:99], v[228:229] op_sel_hi:[1,0,1]
	v_pk_fma_f32 v[140:141], v[140:141], s[98:99], v[230:231] op_sel_hi:[1,0,1]
	v_pk_fma_f32 v[134:135], v[134:135], s[98:99], v[232:233] op_sel_hi:[1,0,1]
	v_pk_fma_f32 v[136:137], v[136:137], s[98:99], v[234:235] op_sel_hi:[1,0,1]
	v_pk_fma_f32 v[130:131], v[130:131], s[98:99], v[236:237] op_sel_hi:[1,0,1]
	v_pk_fma_f32 v[132:133], v[132:133], s[98:99], v[238:239] op_sel_hi:[1,0,1]
	v_min_f32_e32 v142, 0x40e00000, v142
	v_min_f32_e32 v143, 0x40e00000, v143
	v_min_f32_e32 v144, 0x40e00000, v144
	v_min_f32_e32 v145, 0x40e00000, v145
	v_min_f32_e32 v138, 0x40e00000, v138
	v_min_f32_e32 v139, 0x40e00000, v139
	v_min_f32_e32 v140, 0x40e00000, v140
	v_min_f32_e32 v141, 0x40e00000, v141
	v_med3_f32 v134, v134, s59, v189
	v_med3_f32 v135, v135, s59, v189
	v_med3_f32 v136, v136, s59, v189
	v_med3_f32 v137, v137, s59, v189
	v_med3_f32 v130, v130, s59, v189
	v_med3_f32 v131, v131, s59, v189
	v_med3_f32 v132, v132, s59, v189
	v_med3_f32 v133, v133, s59, v189
	v_pk_mul_f32 v[2:3], v[142:143], s[98:99] op_sel:[0,1]
	v_pk_mul_f32 v[4:5], v[144:145], s[98:99] op_sel:[0,1]
	v_pk_mul_f32 v[6:7], v[138:139], s[98:99] op_sel:[0,1]
	v_pk_mul_f32 v[8:9], v[140:141], s[98:99] op_sel:[0,1]
	v_pk_mul_f32 v[2:3], v[2:3], s[100:101] op_sel_hi:[1,0]
	v_pk_mul_f32 v[4:5], v[4:5], s[100:101] op_sel_hi:[1,0]
	v_pk_mul_f32 v[6:7], v[6:7], s[100:101] op_sel_hi:[1,0]
	v_pk_mul_f32 v[8:9], v[8:9], s[100:101] op_sel_hi:[1,0]
	v_exp_f32_e32 v2, v2
	v_exp_f32_e32 v3, v3
	v_exp_f32_e32 v4, v4
	v_exp_f32_e32 v5, v5
	v_exp_f32_e32 v6, v6
	v_exp_f32_e32 v7, v7
	v_exp_f32_e32 v8, v8
	v_exp_f32_e32 v9, v9
	v_pk_fma_f32 v[134:135], v[134:135], s[100:101], v[10:11] op_sel:[0,1,0]
	v_pk_fma_f32 v[136:137], v[136:137], s[100:101], v[10:11] op_sel:[0,1,0]
	v_pk_fma_f32 v[130:131], v[130:131], s[100:101], v[10:11] op_sel:[0,1,0]
	v_pk_fma_f32 v[132:133], v[132:133], s[100:101], v[10:11] op_sel:[0,1,0]
	v_pk_add_f32 v[2:3], v[2:3], v[16:17]
	v_pk_add_f32 v[4:5], v[4:5], v[16:17]
	v_pk_add_f32 v[6:7], v[6:7], v[16:17]
	v_pk_add_f32 v[8:9], v[8:9], v[16:17]
	v_pk_mul_f32 v[142:143], v[142:143], v[134:135]
	v_pk_mul_f32 v[144:145], v[144:145], v[136:137]
	v_pk_mul_f32 v[138:139], v[138:139], v[130:131]
	v_pk_mul_f32 v[140:141], v[140:141], v[132:133]
	v_rcp_f32_e32 v2, v2
	v_rcp_f32_e32 v3, v3
	v_rcp_f32_e32 v4, v4
	v_rcp_f32_e32 v5, v5
	v_rcp_f32_e32 v6, v6
	v_rcp_f32_e32 v7, v7
	v_rcp_f32_e32 v8, v8
	v_rcp_f32_e32 v9, v9
	v_mov_b32_e32 v14, 0x8000
	v_lshl_add_u64 v[20:21], v[18:19], 0, v[14:15]
	v_pk_mul_f32 v[142:143], v[142:143], v[2:3]
	v_pk_mul_f32 v[144:145], v[144:145], v[4:5]
	v_pk_mul_f32 v[138:139], v[138:139], v[6:7]
	v_pk_mul_f32 v[140:141], v[140:141], v[8:9]
	v_cvt_pk_fp8_f32 v22, v142, v143
	v_cvt_pk_fp8_f32 v23, v138, v139
	v_cvt_pk_fp8_f32 v22, v144, v145 op_sel:[0,0,1]
	v_cvt_pk_fp8_f32 v23, v140, v141 op_sel:[0,0,1]
	global_store_dwordx2 v[20:21], v[22:23], off
	v_pk_fma_f32 v[126:127], v[126:127], s[98:99], v[224:225] op_sel_hi:[1,0,1]
	v_pk_fma_f32 v[128:129], v[128:129], s[98:99], v[226:227] op_sel_hi:[1,0,1]
	v_pk_fma_f32 v[122:123], v[122:123], s[98:99], v[228:229] op_sel_hi:[1,0,1]
	v_pk_fma_f32 v[124:125], v[124:125], s[98:99], v[230:231] op_sel_hi:[1,0,1]
	v_pk_fma_f32 v[118:119], v[118:119], s[98:99], v[232:233] op_sel_hi:[1,0,1]
	v_pk_fma_f32 v[120:121], v[120:121], s[98:99], v[234:235] op_sel_hi:[1,0,1]
	v_pk_fma_f32 v[114:115], v[114:115], s[98:99], v[236:237] op_sel_hi:[1,0,1]
	v_pk_fma_f32 v[116:117], v[116:117], s[98:99], v[238:239] op_sel_hi:[1,0,1]
	v_min_f32_e32 v126, 0x40e00000, v126
	v_min_f32_e32 v127, 0x40e00000, v127
	v_min_f32_e32 v128, 0x40e00000, v128
	v_min_f32_e32 v129, 0x40e00000, v129
	v_min_f32_e32 v122, 0x40e00000, v122
	v_min_f32_e32 v123, 0x40e00000, v123
	v_min_f32_e32 v124, 0x40e00000, v124
	v_min_f32_e32 v125, 0x40e00000, v125
	v_med3_f32 v118, v118, s59, v189
	v_med3_f32 v119, v119, s59, v189
	v_med3_f32 v120, v120, s59, v189
	v_med3_f32 v121, v121, s59, v189
	v_med3_f32 v114, v114, s59, v189
	v_med3_f32 v115, v115, s59, v189
	v_med3_f32 v116, v116, s59, v189
	v_med3_f32 v117, v117, s59, v189
	v_pk_mul_f32 v[2:3], v[126:127], s[98:99] op_sel:[0,1]
	v_pk_mul_f32 v[4:5], v[128:129], s[98:99] op_sel:[0,1]
	v_pk_mul_f32 v[6:7], v[122:123], s[98:99] op_sel:[0,1]
	v_pk_mul_f32 v[8:9], v[124:125], s[98:99] op_sel:[0,1]
	v_pk_mul_f32 v[2:3], v[2:3], s[100:101] op_sel_hi:[1,0]
	v_pk_mul_f32 v[4:5], v[4:5], s[100:101] op_sel_hi:[1,0]
	v_pk_mul_f32 v[6:7], v[6:7], s[100:101] op_sel_hi:[1,0]
	v_pk_mul_f32 v[8:9], v[8:9], s[100:101] op_sel_hi:[1,0]
	v_exp_f32_e32 v2, v2
	v_exp_f32_e32 v3, v3
	v_exp_f32_e32 v4, v4
	v_exp_f32_e32 v5, v5
	v_exp_f32_e32 v6, v6
	v_exp_f32_e32 v7, v7
	v_exp_f32_e32 v8, v8
	v_exp_f32_e32 v9, v9
	v_pk_fma_f32 v[118:119], v[118:119], s[100:101], v[10:11] op_sel:[0,1,0]
	v_pk_fma_f32 v[120:121], v[120:121], s[100:101], v[10:11] op_sel:[0,1,0]
	v_pk_fma_f32 v[114:115], v[114:115], s[100:101], v[10:11] op_sel:[0,1,0]
	v_pk_fma_f32 v[116:117], v[116:117], s[100:101], v[10:11] op_sel:[0,1,0]
	v_pk_add_f32 v[2:3], v[2:3], v[16:17]
	v_pk_add_f32 v[4:5], v[4:5], v[16:17]
	v_pk_add_f32 v[6:7], v[6:7], v[16:17]
	v_pk_add_f32 v[8:9], v[8:9], v[16:17]
	v_pk_mul_f32 v[126:127], v[126:127], v[118:119]
	v_pk_mul_f32 v[128:129], v[128:129], v[120:121]
	v_pk_mul_f32 v[122:123], v[122:123], v[114:115]
	v_pk_mul_f32 v[124:125], v[124:125], v[116:117]
	v_rcp_f32_e32 v2, v2
	v_rcp_f32_e32 v3, v3
	v_rcp_f32_e32 v4, v4
	v_rcp_f32_e32 v5, v5
	v_rcp_f32_e32 v6, v6
	v_rcp_f32_e32 v7, v7
	v_rcp_f32_e32 v8, v8
	v_rcp_f32_e32 v9, v9
	v_mov_b32_e32 v14, 0x10000
	v_lshl_add_u64 v[20:21], v[18:19], 0, v[14:15]
	v_pk_mul_f32 v[126:127], v[126:127], v[2:3]
	v_pk_mul_f32 v[128:129], v[128:129], v[4:5]
	v_pk_mul_f32 v[122:123], v[122:123], v[6:7]
	v_pk_mul_f32 v[124:125], v[124:125], v[8:9]
	v_cvt_pk_fp8_f32 v22, v126, v127
	v_cvt_pk_fp8_f32 v23, v122, v123
	v_cvt_pk_fp8_f32 v22, v128, v129 op_sel:[0,0,1]
	v_cvt_pk_fp8_f32 v23, v124, v125 op_sel:[0,0,1]
	global_store_dwordx2 v[20:21], v[22:23], off
	v_pk_fma_f32 v[110:111], v[110:111], s[98:99], v[224:225] op_sel_hi:[1,0,1]
	v_pk_fma_f32 v[112:113], v[112:113], s[98:99], v[226:227] op_sel_hi:[1,0,1]
	v_pk_fma_f32 v[106:107], v[106:107], s[98:99], v[228:229] op_sel_hi:[1,0,1]
	v_pk_fma_f32 v[108:109], v[108:109], s[98:99], v[230:231] op_sel_hi:[1,0,1]
	v_pk_fma_f32 v[102:103], v[102:103], s[98:99], v[232:233] op_sel_hi:[1,0,1]
	v_pk_fma_f32 v[104:105], v[104:105], s[98:99], v[234:235] op_sel_hi:[1,0,1]
	v_pk_fma_f32 v[98:99], v[98:99], s[98:99], v[236:237] op_sel_hi:[1,0,1]
	v_pk_fma_f32 v[100:101], v[100:101], s[98:99], v[238:239] op_sel_hi:[1,0,1]
	v_min_f32_e32 v110, 0x40e00000, v110
	v_min_f32_e32 v111, 0x40e00000, v111
	v_min_f32_e32 v112, 0x40e00000, v112
	v_min_f32_e32 v113, 0x40e00000, v113
	v_min_f32_e32 v106, 0x40e00000, v106
	v_min_f32_e32 v107, 0x40e00000, v107
	v_min_f32_e32 v108, 0x40e00000, v108
	v_min_f32_e32 v109, 0x40e00000, v109
	v_med3_f32 v102, v102, s59, v189
	v_med3_f32 v103, v103, s59, v189
	v_med3_f32 v104, v104, s59, v189
	v_med3_f32 v105, v105, s59, v189
	v_med3_f32 v98, v98, s59, v189
	v_med3_f32 v99, v99, s59, v189
	v_med3_f32 v100, v100, s59, v189
	v_med3_f32 v101, v101, s59, v189
	v_pk_mul_f32 v[2:3], v[110:111], s[98:99] op_sel:[0,1]
	v_pk_mul_f32 v[4:5], v[112:113], s[98:99] op_sel:[0,1]
	v_pk_mul_f32 v[6:7], v[106:107], s[98:99] op_sel:[0,1]
	v_pk_mul_f32 v[8:9], v[108:109], s[98:99] op_sel:[0,1]
	v_pk_mul_f32 v[2:3], v[2:3], s[100:101] op_sel_hi:[1,0]
	v_pk_mul_f32 v[4:5], v[4:5], s[100:101] op_sel_hi:[1,0]
	v_pk_mul_f32 v[6:7], v[6:7], s[100:101] op_sel_hi:[1,0]
	v_pk_mul_f32 v[8:9], v[8:9], s[100:101] op_sel_hi:[1,0]
	v_exp_f32_e32 v2, v2
	v_exp_f32_e32 v3, v3
	v_exp_f32_e32 v4, v4
	v_exp_f32_e32 v5, v5
	v_exp_f32_e32 v6, v6
	v_exp_f32_e32 v7, v7
	v_exp_f32_e32 v8, v8
	v_exp_f32_e32 v9, v9
	v_pk_fma_f32 v[102:103], v[102:103], s[100:101], v[10:11] op_sel:[0,1,0]
	v_pk_fma_f32 v[104:105], v[104:105], s[100:101], v[10:11] op_sel:[0,1,0]
	v_pk_fma_f32 v[98:99], v[98:99], s[100:101], v[10:11] op_sel:[0,1,0]
	v_pk_fma_f32 v[100:101], v[100:101], s[100:101], v[10:11] op_sel:[0,1,0]
	v_pk_add_f32 v[2:3], v[2:3], v[16:17]
	v_pk_add_f32 v[4:5], v[4:5], v[16:17]
	v_pk_add_f32 v[6:7], v[6:7], v[16:17]
	v_pk_add_f32 v[8:9], v[8:9], v[16:17]
	v_pk_mul_f32 v[110:111], v[110:111], v[102:103]
	v_pk_mul_f32 v[112:113], v[112:113], v[104:105]
	v_pk_mul_f32 v[106:107], v[106:107], v[98:99]
	v_pk_mul_f32 v[108:109], v[108:109], v[100:101]
	v_rcp_f32_e32 v2, v2
	v_rcp_f32_e32 v3, v3
	v_rcp_f32_e32 v4, v4
	v_rcp_f32_e32 v5, v5
	v_rcp_f32_e32 v6, v6
	v_rcp_f32_e32 v7, v7
	v_rcp_f32_e32 v8, v8
	v_rcp_f32_e32 v9, v9
	v_mov_b32_e32 v14, 0x18000
	v_lshl_add_u64 v[20:21], v[18:19], 0, v[14:15]
	v_pk_mul_f32 v[110:111], v[110:111], v[2:3]
	v_pk_mul_f32 v[112:113], v[112:113], v[4:5]
	v_pk_mul_f32 v[106:107], v[106:107], v[6:7]
	v_pk_mul_f32 v[108:109], v[108:109], v[8:9]
	v_cvt_pk_fp8_f32 v22, v110, v111
	v_cvt_pk_fp8_f32 v23, v106, v107
	v_cvt_pk_fp8_f32 v22, v112, v113 op_sel:[0,0,1]
	v_cvt_pk_fp8_f32 v23, v108, v109 op_sel:[0,0,1]
	global_store_dwordx2 v[20:21], v[22:23], off
	v_pk_fma_f32 v[94:95], v[94:95], s[98:99], v[224:225] op_sel_hi:[1,0,1]
	v_pk_fma_f32 v[96:97], v[96:97], s[98:99], v[226:227] op_sel_hi:[1,0,1]
	v_pk_fma_f32 v[90:91], v[90:91], s[98:99], v[228:229] op_sel_hi:[1,0,1]
	v_pk_fma_f32 v[92:93], v[92:93], s[98:99], v[230:231] op_sel_hi:[1,0,1]
	v_pk_fma_f32 v[86:87], v[86:87], s[98:99], v[232:233] op_sel_hi:[1,0,1]
	v_pk_fma_f32 v[88:89], v[88:89], s[98:99], v[234:235] op_sel_hi:[1,0,1]
	v_pk_fma_f32 v[82:83], v[82:83], s[98:99], v[236:237] op_sel_hi:[1,0,1]
	v_pk_fma_f32 v[84:85], v[84:85], s[98:99], v[238:239] op_sel_hi:[1,0,1]
	v_min_f32_e32 v94, 0x40e00000, v94
	v_min_f32_e32 v95, 0x40e00000, v95
	v_min_f32_e32 v96, 0x40e00000, v96
	v_min_f32_e32 v97, 0x40e00000, v97
	v_min_f32_e32 v90, 0x40e00000, v90
	v_min_f32_e32 v91, 0x40e00000, v91
	v_min_f32_e32 v92, 0x40e00000, v92
	v_min_f32_e32 v93, 0x40e00000, v93
	v_med3_f32 v86, v86, s59, v189
	v_med3_f32 v87, v87, s59, v189
	v_med3_f32 v88, v88, s59, v189
	v_med3_f32 v89, v89, s59, v189
	v_med3_f32 v82, v82, s59, v189
	v_med3_f32 v83, v83, s59, v189
	v_med3_f32 v84, v84, s59, v189
	v_med3_f32 v85, v85, s59, v189
	v_pk_mul_f32 v[2:3], v[94:95], s[98:99] op_sel:[0,1]
	v_pk_mul_f32 v[4:5], v[96:97], s[98:99] op_sel:[0,1]
	v_pk_mul_f32 v[6:7], v[90:91], s[98:99] op_sel:[0,1]
	v_pk_mul_f32 v[8:9], v[92:93], s[98:99] op_sel:[0,1]
	v_pk_mul_f32 v[2:3], v[2:3], s[100:101] op_sel_hi:[1,0]
	v_pk_mul_f32 v[4:5], v[4:5], s[100:101] op_sel_hi:[1,0]
	v_pk_mul_f32 v[6:7], v[6:7], s[100:101] op_sel_hi:[1,0]
	v_pk_mul_f32 v[8:9], v[8:9], s[100:101] op_sel_hi:[1,0]
	v_exp_f32_e32 v2, v2
	v_exp_f32_e32 v3, v3
	v_exp_f32_e32 v4, v4
	v_exp_f32_e32 v5, v5
	v_exp_f32_e32 v6, v6
	v_exp_f32_e32 v7, v7
	v_exp_f32_e32 v8, v8
	v_exp_f32_e32 v9, v9
	v_pk_fma_f32 v[86:87], v[86:87], s[100:101], v[10:11] op_sel:[0,1,0]
	v_pk_fma_f32 v[88:89], v[88:89], s[100:101], v[10:11] op_sel:[0,1,0]
	v_pk_fma_f32 v[82:83], v[82:83], s[100:101], v[10:11] op_sel:[0,1,0]
	v_pk_fma_f32 v[84:85], v[84:85], s[100:101], v[10:11] op_sel:[0,1,0]
	v_pk_add_f32 v[2:3], v[2:3], v[16:17]
	v_pk_add_f32 v[4:5], v[4:5], v[16:17]
	v_pk_add_f32 v[6:7], v[6:7], v[16:17]
	v_pk_add_f32 v[8:9], v[8:9], v[16:17]
	v_pk_mul_f32 v[94:95], v[94:95], v[86:87]
	v_pk_mul_f32 v[96:97], v[96:97], v[88:89]
	v_pk_mul_f32 v[90:91], v[90:91], v[82:83]
	v_pk_mul_f32 v[92:93], v[92:93], v[84:85]
	v_rcp_f32_e32 v2, v2
	v_rcp_f32_e32 v3, v3
	v_rcp_f32_e32 v4, v4
	v_rcp_f32_e32 v5, v5
	v_rcp_f32_e32 v6, v6
	v_rcp_f32_e32 v7, v7
	v_rcp_f32_e32 v8, v8
	v_rcp_f32_e32 v9, v9
	v_mov_b32_e32 v14, 0x40000
	v_lshl_add_u64 v[20:21], v[18:19], 0, v[14:15]
	v_pk_mul_f32 v[94:95], v[94:95], v[2:3]
	v_pk_mul_f32 v[96:97], v[96:97], v[4:5]
	v_pk_mul_f32 v[90:91], v[90:91], v[6:7]
	v_pk_mul_f32 v[92:93], v[92:93], v[8:9]
	v_cvt_pk_fp8_f32 v22, v94, v95
	v_cvt_pk_fp8_f32 v23, v90, v91
	v_cvt_pk_fp8_f32 v22, v96, v97 op_sel:[0,0,1]
	v_cvt_pk_fp8_f32 v23, v92, v93 op_sel:[0,0,1]
	global_store_dwordx2 v[20:21], v[22:23], off
	v_pk_fma_f32 v[78:79], v[78:79], s[98:99], v[224:225] op_sel_hi:[1,0,1]
	v_pk_fma_f32 v[80:81], v[80:81], s[98:99], v[226:227] op_sel_hi:[1,0,1]
	v_pk_fma_f32 v[74:75], v[74:75], s[98:99], v[228:229] op_sel_hi:[1,0,1]
	v_pk_fma_f32 v[76:77], v[76:77], s[98:99], v[230:231] op_sel_hi:[1,0,1]
	v_pk_fma_f32 v[70:71], v[70:71], s[98:99], v[232:233] op_sel_hi:[1,0,1]
	v_pk_fma_f32 v[72:73], v[72:73], s[98:99], v[234:235] op_sel_hi:[1,0,1]
	v_pk_fma_f32 v[66:67], v[66:67], s[98:99], v[236:237] op_sel_hi:[1,0,1]
	v_pk_fma_f32 v[68:69], v[68:69], s[98:99], v[238:239] op_sel_hi:[1,0,1]
	v_min_f32_e32 v78, 0x40e00000, v78
	v_min_f32_e32 v79, 0x40e00000, v79
	v_min_f32_e32 v80, 0x40e00000, v80
	v_min_f32_e32 v81, 0x40e00000, v81
	v_min_f32_e32 v74, 0x40e00000, v74
	v_min_f32_e32 v75, 0x40e00000, v75
	v_min_f32_e32 v76, 0x40e00000, v76
	v_min_f32_e32 v77, 0x40e00000, v77
	v_med3_f32 v70, v70, s59, v189
	v_med3_f32 v71, v71, s59, v189
	v_med3_f32 v72, v72, s59, v189
	v_med3_f32 v73, v73, s59, v189
	v_med3_f32 v66, v66, s59, v189
	v_med3_f32 v67, v67, s59, v189
	v_med3_f32 v68, v68, s59, v189
	v_med3_f32 v69, v69, s59, v189
	v_pk_mul_f32 v[2:3], v[78:79], s[98:99] op_sel:[0,1]
	v_pk_mul_f32 v[4:5], v[80:81], s[98:99] op_sel:[0,1]
	v_pk_mul_f32 v[6:7], v[74:75], s[98:99] op_sel:[0,1]
	v_pk_mul_f32 v[8:9], v[76:77], s[98:99] op_sel:[0,1]
	v_pk_mul_f32 v[2:3], v[2:3], s[100:101] op_sel_hi:[1,0]
	v_pk_mul_f32 v[4:5], v[4:5], s[100:101] op_sel_hi:[1,0]
	v_pk_mul_f32 v[6:7], v[6:7], s[100:101] op_sel_hi:[1,0]
	v_pk_mul_f32 v[8:9], v[8:9], s[100:101] op_sel_hi:[1,0]
	v_exp_f32_e32 v2, v2
	v_exp_f32_e32 v3, v3
	v_exp_f32_e32 v4, v4
	v_exp_f32_e32 v5, v5
	v_exp_f32_e32 v6, v6
	v_exp_f32_e32 v7, v7
	v_exp_f32_e32 v8, v8
	v_exp_f32_e32 v9, v9
	v_pk_fma_f32 v[70:71], v[70:71], s[100:101], v[10:11] op_sel:[0,1,0]
	v_pk_fma_f32 v[72:73], v[72:73], s[100:101], v[10:11] op_sel:[0,1,0]
	v_pk_fma_f32 v[66:67], v[66:67], s[100:101], v[10:11] op_sel:[0,1,0]
	v_pk_fma_f32 v[68:69], v[68:69], s[100:101], v[10:11] op_sel:[0,1,0]
	v_pk_add_f32 v[2:3], v[2:3], v[16:17]
	v_pk_add_f32 v[4:5], v[4:5], v[16:17]
	v_pk_add_f32 v[6:7], v[6:7], v[16:17]
	v_pk_add_f32 v[8:9], v[8:9], v[16:17]
	v_pk_mul_f32 v[78:79], v[78:79], v[70:71]
	v_pk_mul_f32 v[80:81], v[80:81], v[72:73]
	v_pk_mul_f32 v[74:75], v[74:75], v[66:67]
	v_pk_mul_f32 v[76:77], v[76:77], v[68:69]
	v_rcp_f32_e32 v2, v2
	v_rcp_f32_e32 v3, v3
	v_rcp_f32_e32 v4, v4
	v_rcp_f32_e32 v5, v5
	v_rcp_f32_e32 v6, v6
	v_rcp_f32_e32 v7, v7
	v_rcp_f32_e32 v8, v8
	v_rcp_f32_e32 v9, v9
	v_mov_b32_e32 v14, 0x48000
	v_lshl_add_u64 v[20:21], v[18:19], 0, v[14:15]
	v_pk_mul_f32 v[78:79], v[78:79], v[2:3]
	v_pk_mul_f32 v[80:81], v[80:81], v[4:5]
	v_pk_mul_f32 v[74:75], v[74:75], v[6:7]
	v_pk_mul_f32 v[76:77], v[76:77], v[8:9]
	v_cvt_pk_fp8_f32 v22, v78, v79
	v_cvt_pk_fp8_f32 v23, v74, v75
	v_cvt_pk_fp8_f32 v22, v80, v81 op_sel:[0,0,1]
	v_cvt_pk_fp8_f32 v23, v76, v77 op_sel:[0,0,1]
	global_store_dwordx2 v[20:21], v[22:23], off
	v_pk_fma_f32 v[62:63], v[62:63], s[98:99], v[224:225] op_sel_hi:[1,0,1]
	v_pk_fma_f32 v[64:65], v[64:65], s[98:99], v[226:227] op_sel_hi:[1,0,1]
	v_pk_fma_f32 v[58:59], v[58:59], s[98:99], v[228:229] op_sel_hi:[1,0,1]
	v_pk_fma_f32 v[60:61], v[60:61], s[98:99], v[230:231] op_sel_hi:[1,0,1]
	v_pk_fma_f32 v[54:55], v[54:55], s[98:99], v[232:233] op_sel_hi:[1,0,1]
	v_pk_fma_f32 v[56:57], v[56:57], s[98:99], v[234:235] op_sel_hi:[1,0,1]
	v_pk_fma_f32 v[50:51], v[50:51], s[98:99], v[236:237] op_sel_hi:[1,0,1]
	v_pk_fma_f32 v[52:53], v[52:53], s[98:99], v[238:239] op_sel_hi:[1,0,1]
	v_min_f32_e32 v62, 0x40e00000, v62
	v_min_f32_e32 v63, 0x40e00000, v63
	v_min_f32_e32 v64, 0x40e00000, v64
	v_min_f32_e32 v65, 0x40e00000, v65
	v_min_f32_e32 v58, 0x40e00000, v58
	v_min_f32_e32 v59, 0x40e00000, v59
	v_min_f32_e32 v60, 0x40e00000, v60
	v_min_f32_e32 v61, 0x40e00000, v61
	v_med3_f32 v54, v54, s59, v189
	v_med3_f32 v55, v55, s59, v189
	v_med3_f32 v56, v56, s59, v189
	v_med3_f32 v57, v57, s59, v189
	v_med3_f32 v50, v50, s59, v189
	v_med3_f32 v51, v51, s59, v189
	v_med3_f32 v52, v52, s59, v189
	v_med3_f32 v53, v53, s59, v189
	v_pk_mul_f32 v[2:3], v[62:63], s[98:99] op_sel:[0,1]
	v_pk_mul_f32 v[4:5], v[64:65], s[98:99] op_sel:[0,1]
	v_pk_mul_f32 v[6:7], v[58:59], s[98:99] op_sel:[0,1]
	v_pk_mul_f32 v[8:9], v[60:61], s[98:99] op_sel:[0,1]
	v_pk_mul_f32 v[2:3], v[2:3], s[100:101] op_sel_hi:[1,0]
	v_pk_mul_f32 v[4:5], v[4:5], s[100:101] op_sel_hi:[1,0]
	v_pk_mul_f32 v[6:7], v[6:7], s[100:101] op_sel_hi:[1,0]
	v_pk_mul_f32 v[8:9], v[8:9], s[100:101] op_sel_hi:[1,0]
	v_exp_f32_e32 v2, v2
	v_exp_f32_e32 v3, v3
	v_exp_f32_e32 v4, v4
	v_exp_f32_e32 v5, v5
	v_exp_f32_e32 v6, v6
	v_exp_f32_e32 v7, v7
	v_exp_f32_e32 v8, v8
	v_exp_f32_e32 v9, v9
	v_pk_fma_f32 v[54:55], v[54:55], s[100:101], v[10:11] op_sel:[0,1,0]
	v_pk_fma_f32 v[56:57], v[56:57], s[100:101], v[10:11] op_sel:[0,1,0]
	v_pk_fma_f32 v[50:51], v[50:51], s[100:101], v[10:11] op_sel:[0,1,0]
	v_pk_fma_f32 v[52:53], v[52:53], s[100:101], v[10:11] op_sel:[0,1,0]
	v_pk_add_f32 v[2:3], v[2:3], v[16:17]
	v_pk_add_f32 v[4:5], v[4:5], v[16:17]
	v_pk_add_f32 v[6:7], v[6:7], v[16:17]
	v_pk_add_f32 v[8:9], v[8:9], v[16:17]
	v_pk_mul_f32 v[62:63], v[62:63], v[54:55]
	v_pk_mul_f32 v[64:65], v[64:65], v[56:57]
	v_pk_mul_f32 v[58:59], v[58:59], v[50:51]
	v_pk_mul_f32 v[60:61], v[60:61], v[52:53]
	v_rcp_f32_e32 v2, v2
	v_rcp_f32_e32 v3, v3
	v_rcp_f32_e32 v4, v4
	v_rcp_f32_e32 v5, v5
	v_rcp_f32_e32 v6, v6
	v_rcp_f32_e32 v7, v7
	v_rcp_f32_e32 v8, v8
	v_rcp_f32_e32 v9, v9
	v_mov_b32_e32 v14, 0x50000
	v_lshl_add_u64 v[20:21], v[18:19], 0, v[14:15]
	v_pk_mul_f32 v[62:63], v[62:63], v[2:3]
	v_pk_mul_f32 v[64:65], v[64:65], v[4:5]
	v_pk_mul_f32 v[58:59], v[58:59], v[6:7]
	v_pk_mul_f32 v[60:61], v[60:61], v[8:9]
	v_cvt_pk_fp8_f32 v22, v62, v63
	v_cvt_pk_fp8_f32 v23, v58, v59
	v_cvt_pk_fp8_f32 v22, v64, v65 op_sel:[0,0,1]
	v_cvt_pk_fp8_f32 v23, v60, v61 op_sel:[0,0,1]
	global_store_dwordx2 v[20:21], v[22:23], off
	v_pk_fma_f32 v[46:47], v[46:47], s[98:99], v[224:225] op_sel_hi:[1,0,1]
	v_pk_fma_f32 v[48:49], v[48:49], s[98:99], v[226:227] op_sel_hi:[1,0,1]
	v_pk_fma_f32 v[42:43], v[42:43], s[98:99], v[228:229] op_sel_hi:[1,0,1]
	v_pk_fma_f32 v[44:45], v[44:45], s[98:99], v[230:231] op_sel_hi:[1,0,1]
	v_pk_fma_f32 v[38:39], v[38:39], s[98:99], v[232:233] op_sel_hi:[1,0,1]
	v_pk_fma_f32 v[40:41], v[40:41], s[98:99], v[234:235] op_sel_hi:[1,0,1]
	v_pk_fma_f32 v[34:35], v[34:35], s[98:99], v[236:237] op_sel_hi:[1,0,1]
	v_pk_fma_f32 v[36:37], v[36:37], s[98:99], v[238:239] op_sel_hi:[1,0,1]
	v_min_f32_e32 v46, 0x40e00000, v46
	v_min_f32_e32 v47, 0x40e00000, v47
	v_min_f32_e32 v48, 0x40e00000, v48
	v_min_f32_e32 v49, 0x40e00000, v49
	v_min_f32_e32 v42, 0x40e00000, v42
	v_min_f32_e32 v43, 0x40e00000, v43
	v_min_f32_e32 v44, 0x40e00000, v44
	v_min_f32_e32 v45, 0x40e00000, v45
	v_med3_f32 v38, v38, s59, v189
	v_med3_f32 v39, v39, s59, v189
	v_med3_f32 v40, v40, s59, v189
	v_med3_f32 v41, v41, s59, v189
	v_med3_f32 v34, v34, s59, v189
	v_med3_f32 v35, v35, s59, v189
	v_med3_f32 v36, v36, s59, v189
	v_med3_f32 v37, v37, s59, v189
	v_pk_mul_f32 v[2:3], v[46:47], s[98:99] op_sel:[0,1]
	v_pk_mul_f32 v[4:5], v[48:49], s[98:99] op_sel:[0,1]
	v_pk_mul_f32 v[6:7], v[42:43], s[98:99] op_sel:[0,1]
	v_pk_mul_f32 v[8:9], v[44:45], s[98:99] op_sel:[0,1]
	v_pk_mul_f32 v[2:3], v[2:3], s[100:101] op_sel_hi:[1,0]
	v_pk_mul_f32 v[4:5], v[4:5], s[100:101] op_sel_hi:[1,0]
	v_pk_mul_f32 v[6:7], v[6:7], s[100:101] op_sel_hi:[1,0]
	v_pk_mul_f32 v[8:9], v[8:9], s[100:101] op_sel_hi:[1,0]
	v_exp_f32_e32 v2, v2
	v_exp_f32_e32 v3, v3
	v_exp_f32_e32 v4, v4
	v_exp_f32_e32 v5, v5
	v_exp_f32_e32 v6, v6
	v_exp_f32_e32 v7, v7
	v_exp_f32_e32 v8, v8
	v_exp_f32_e32 v9, v9
	v_pk_fma_f32 v[38:39], v[38:39], s[100:101], v[10:11] op_sel:[0,1,0]
	v_pk_fma_f32 v[40:41], v[40:41], s[100:101], v[10:11] op_sel:[0,1,0]
	v_pk_fma_f32 v[34:35], v[34:35], s[100:101], v[10:11] op_sel:[0,1,0]
	v_pk_fma_f32 v[36:37], v[36:37], s[100:101], v[10:11] op_sel:[0,1,0]
	v_pk_add_f32 v[2:3], v[2:3], v[16:17]
	v_pk_add_f32 v[4:5], v[4:5], v[16:17]
	v_pk_add_f32 v[6:7], v[6:7], v[16:17]
	v_pk_add_f32 v[8:9], v[8:9], v[16:17]
	v_pk_mul_f32 v[46:47], v[46:47], v[38:39]
	v_pk_mul_f32 v[48:49], v[48:49], v[40:41]
	v_pk_mul_f32 v[42:43], v[42:43], v[34:35]
	v_pk_mul_f32 v[44:45], v[44:45], v[36:37]
	v_rcp_f32_e32 v2, v2
	v_rcp_f32_e32 v3, v3
	v_rcp_f32_e32 v4, v4
	v_rcp_f32_e32 v5, v5
	v_rcp_f32_e32 v6, v6
	v_rcp_f32_e32 v7, v7
	v_rcp_f32_e32 v8, v8
	v_rcp_f32_e32 v9, v9
	v_mov_b32_e32 v14, 0x58000
	v_lshl_add_u64 v[20:21], v[18:19], 0, v[14:15]
	v_pk_mul_f32 v[46:47], v[46:47], v[2:3]
	v_pk_mul_f32 v[48:49], v[48:49], v[4:5]
	v_pk_mul_f32 v[42:43], v[42:43], v[6:7]
	v_pk_mul_f32 v[44:45], v[44:45], v[8:9]
	v_cvt_pk_fp8_f32 v22, v46, v47
	v_cvt_pk_fp8_f32 v23, v42, v43
	v_cvt_pk_fp8_f32 v22, v48, v49 op_sel:[0,0,1]
	v_cvt_pk_fp8_f32 v23, v44, v45 op_sel:[0,0,1]
	s_andn2_b64 vcc, exec, s[4:5]
	s_mov_b64 s[4:5], -1
	global_store_dwordx2 v[20:21], v[22:23], off
	s_cbranch_vccnz .LBB0_1470
	s_andn2_b64 vcc, exec, s[12:13]
	s_cbranch_vccnz .LBB0_1469
	s_barrier
	s_branch .LBB0_1469
